# SSD scan (both copies): chunk-loop head waits (vmcnt 0/14/10/9, needed only on the first trip) dropped; the unit prologue drains its loads once instead, so later trips no longer wait on the next chunk
# speedup vs baseline: 1.0004x; 1.0004x over previous
; #define LAS __attribute__((address_space(3)))
; __device__ __forceinline__ void ssd_scan_phase(LAS unsigned char* lds, const bf16_t* xbcc, const float* dtb, const float* a_log, const float* dskip, bf16_t* yssd, const int vcu, const int G, const int tid) {
;     ...
;     for (int u = vcu; u < BATCH * SSD_H * 2; u += G) {
;         const int b = u >> 5, h = (u >> 1) & 15, phalf = u & 1, g = h >> 3;
;         const float Ah = -expf(a_log[h]) * 1.4426950408889634f;
;         const float dsk = dskip[h];
;         f32x4 hs[2] = {(f32x4){0.f, 0.f, 0.f, 0.f}, (f32x4){0.f, 0.f, 0.f, 0.f}};
;         for (int i = tid; i < 32 * SP / 2; i += 512) ((LAS unsigned*)hT)[i] = 0u;
;         const int row = tid >> 2, part = tid & 3;
;         u32x4 cvn[4], bvn[4], xrn; float dtn = 0.f, dtn1 = 0.f;
;     ...
;         SS_FETCH(0);
.LBB0_667:
	s_or_b64 exec, exec, s[34:35]
	s_waitcnt vmcnt(10)
	v_mul_f32_e32 v5, 0x3fb8aa3b, v4
	v_rndne_f32_e32 v6, v5
	s_mov_b32 s34, 0x3fb8aa3b
	v_sub_f32_e32 v7, v5, v6
	v_fma_f32 v5, v4, s34, -v5
	v_fmac_f32_e32 v5, 0x32a5705f, v4
	v_add_f32_e32 v5, v7, v5
	v_exp_f32_e32 v5, v5
	v_cvt_i32_f32_e32 v6, v6
	s_and_b32 s31, s37, 0xfffff800
	s_lshl_b32 s29, s36, 6
	v_add_u32_e32 v149, s31, v113
	v_add_u32_e32 v150, s31, v141
	v_add_u32_e32 v151, s31, v142
	s_mov_b32 s31, 0xc2ce8ed0
	v_readlane_b32 s34, v254, 33
	v_ldexp_f32 v5, v5, v6
	v_cmp_ngt_f32_e32 vcc, s31, v4
	s_mov_b32 s31, 0x42b17218
	v_readlane_b32 s35, v254, 34
	s_add_u32 s30, s34, s30
	v_cndmask_b32_e32 v5, 0, v5, vcc
	v_cmp_nlt_f32_e32 vcc, s31, v4
	s_addc_u32 s31, s35, 0
	s_lshl_b32 s34, s29, 1
	v_readlane_b32 s29, v254, 40
	s_add_u32 s29, s29, s34
	v_readlane_b32 s35, v254, 42
	s_addc_u32 s35, s35, 0
	s_add_u32 s36, s29, s28
	v_writelane_b32 v255, s37, 12
	v_cndmask_b32_e32 v4, v242, v5, vcc
	s_addc_u32 s37, s35, 0
	v_mov_b32_e32 v99, v3
	v_mul_f32_e32 v152, 0xbfb8aa3b, v4
	v_lshl_add_u64 v[104:105], s[36:37], 0, v[98:99]
	s_waitcnt vmcnt(9)
	v_mov_b32_e32 v101, v100
	s_mov_b32 s36, 0
	v_mov_b32_e32 v41, v40
	v_mov_b32_e32 v42, v40
	v_mov_b32_e32 v43, v40
	v_mov_b32_e32 v44, v40
	v_mov_b32_e32 v45, v40
	v_mov_b32_e32 v46, v40
	v_mov_b32_e32 v47, v40
	s_movk_i32 s97, 0x3000
	s_waitcnt vmcnt(0)
	s_branch .LBB0_669

; #define LAS __attribute__((address_space(3)))
; #define SS_DPPF(x_, ctrl_, rm_, bc_) __int_as_float(__builtin_amdgcn_update_dpp(0, __float_as_int(x_), (ctrl_), (rm_), 0xF, (bc_)))
; __device__ __forceinline__ void ssd_scan_phase(LAS unsigned char* lds, const bf16_t* xbcc, const float* dtb, const float* a_log, const float* dskip, bf16_t* yssd, const int vcu, const int G, const int tid) {
;     ...
;                 if (wave == 0) {
;                     const float d0 = dtn, d1 = dtn1;
;                     *(LAS f32x2*)(dtv + 2 * lane) = (f32x2){d0, d1};
;                     const float v0 = d0 * Ah, v1 = d1 * Ah;
;                     float s = v0 + v1;
;     ...
;                     s += SS_DPPF(s, 0x111, 0xF, true); asm("" : "+v"(s));
;                     s += SS_DPPF(s, 0x112, 0xF, true); asm("" : "+v"(s));
;                     s += SS_DPPF(s, 0x114, 0xF, true); asm("" : "+v"(s));
;                     s += SS_DPPF(s, 0x118, 0xF, true); asm("" : "+v"(s));
;                     s += SS_DPPF(s, 0x142, 0xA, false); asm("" : "+v"(s));
;                     s += SS_DPPF(s, 0x143, 0xC, false); asm("" : "+v"(s));
;     ...
;                     *(LAS f32x2*)(acum + 2 * lane) = (f32x2){s - v1, s};
;                 }
.LBB0_669:
	s_andn2_b64 vcc, exec, s[2:3]
	s_cbranch_vccnz .LBB0_671
	v_mul_f32_e32 v4, v152, v103
	v_fmac_f32_e32 v4, v152, v102
	v_mov_b32_e32 v5, v3
	ds_write_b64 v108, v[102:103]
	v_add_f32_dpp v4, v4, v4 row_shr:1 row_mask:0xf bank_mask:0xf bound_ctrl:1
	s_nop 1
	v_add_f32_dpp v4, v4, v4 row_shr:2 row_mask:0xf bank_mask:0xf bound_ctrl:1
	s_nop 1
	v_add_f32_dpp v4, v4, v4 row_shr:4 row_mask:0xf bank_mask:0xf bound_ctrl:1
	s_nop 1
	v_add_f32_dpp v4, v4, v4 row_shr:8 row_mask:0xf bank_mask:0xf bound_ctrl:1
	s_nop 1
	v_mov_b32_dpp v5, v4 row_bcast:15 row_mask:0xa bank_mask:0xf
	v_add_f32_e32 v4, v4, v5
	v_mov_b32_e32 v5, v3
	s_nop 1
	v_mov_b32_dpp v5, v4 row_bcast:31 row_mask:0xc bank_mask:0xf
	v_add_f32_e32 v5, v4, v5
	s_nop 0
	v_fma_f32 v4, -v152, v103, v5
	ds_write_b64 v109, v[4:5]

; #define LAS __attribute__((address_space(3)))
; __device__ __forceinline__ unsigned cvt_pk_bf16(float lo, float hi) { const f32x2 v = {lo, hi}; const bf16x2_t b = __builtin_convertvector(v, bf16x2_t); return __builtin_bit_cast(unsigned, b); }
; __device__ __forceinline__ void ssd_scan_phase(LAS unsigned char* lds, const bf16_t* xbcc, const float* dtb, const float* a_log, const float* dskip, bf16_t* yssd, const int vcu, const int G, const int tid) {
;     ...
;                 for (int j = 0; j < 4; ++j) { *(LAS u32x4*)(Cimg + row * SP + 32 * part + 8 * j) = cv[j]; *(LAS u32x4*)(Bimg + row * SP + 32 * part + 8 * j) = bv[j]; }
; #pragma unroll
;                 for (int j = 0; j < 4; ++j) { const unsigned wv[4] = {bv[j].x, bv[j].y, bv[j].z, bv[j].w};
; #pragma unroll
;                     for (int e = 0; e < 4; ++e) { const int n = 32 * part + 8 * j + 2 * e; BTimg[n * SP + row] = (bf16_t)(wv[e] & 0xffffu); BTimg[(n + 1) * SP + row] = (bf16_t)(wv[e] >> 16); } }
;             }
;             __syncthreads();
;             const float atot = acum[127];
;             {
;                 const float wgt = dtv[row] * __builtin_amdgcn_exp2f(atot - acum[row]);
;                 const unsigned wv[4] = {xr.x, xr.y, xr.z, xr.w};
; #pragma unroll
;                 for (int e = 0; e < 4; ++e) { const int p = 8 * part + 2 * e; const float x0 = bf_lo(wv[e]), x1 = bf_hi(wv[e]);
;                     xT[p * SP + row] = (bf16_t)(wv[e] & 0xffffu); xT[(p + 1) * SP + row] = (bf16_t)(wv[e] >> 16);
;                     const unsigned pk = cvt_pk_bf16(x0 * wgt, x1 * wgt); xwT[p * SP + row] = (bf16_t)(pk & 0xffffu); xwT[(p + 1) * SP + row] = (bf16_t)(pk >> 16); }
;             }
;             f32x4 gacc[8];
; #pragma unroll
;             for (int st = 0; st < 8; ++st) gacc[st] = (f32x4){0.f, 0.f, 0.f, 0.f};
;             {
;                 bf16x8 cf[4];
; #pragma unroll
;                 for (int ks = 0; ks < 4; ++ks) cf[ks] = *(const LAS bf16x8*)(Cimg + (16 * lt + fr) * SP + 32 * ks + 8 * fq);
; #pragma unroll
;                 for (int st = 0; st < 8; ++st) if (st <= lt) {
; #pragma unroll
;                     for (int ks = 0; ks < 4; ++ks) { const bf16x8 bfg = *(const LAS bf16x8*)(Bimg + (16 * st + fr) * SP + 32 * ks + 8 * fq);
;                         gacc[st] = __builtin_amdgcn_mfma_f32_16x16x32_bf16(bfg, cf[ks], gacc[st], 0, 0, 0); }
.LBB0_676:
	v_readlane_b32 s29, v253, 56
	ds_write_b128 v110, v[80:83]
	ds_write_b128 v110, v[64:67] offset:34816
	ds_write_b128 v110, v[76:79] offset:16
	ds_write_b128 v110, v[60:63] offset:34832
	ds_write_b128 v110, v[72:75] offset:32
	ds_write_b128 v110, v[56:59] offset:34848
	ds_write_b128 v110, v[68:71] offset:48
	ds_write_b128 v110, v[52:55] offset:34864
	ds_write_b16 v122, v64
	ds_write_b16_d16_hi v122, v64 offset:272
	ds_write_b16 v122, v65 offset:544
	ds_write_b16_d16_hi v122, v65 offset:816
	ds_write_b16 v122, v66 offset:1088
	ds_write_b16_d16_hi v122, v66 offset:1360
	ds_write_b16 v122, v67 offset:1632
	ds_write_b16_d16_hi v122, v67 offset:1904
	ds_write_b16 v122, v60 offset:2176
	ds_write_b16_d16_hi v122, v60 offset:2448
	ds_write_b16 v122, v61 offset:2720
	ds_write_b16_d16_hi v122, v61 offset:2992
	ds_write_b16 v122, v62 offset:3264
	ds_write_b16_d16_hi v122, v62 offset:3536
	ds_write_b16 v122, v63 offset:3808
	ds_write_b16_d16_hi v122, v63 offset:4080
	ds_write_b16 v122, v56 offset:4352
	ds_write_b16_d16_hi v122, v56 offset:4624
	ds_write_b16 v122, v57 offset:4896
	ds_write_b16_d16_hi v122, v57 offset:5168
	ds_write_b16 v122, v58 offset:5440
	ds_write_b16_d16_hi v122, v58 offset:5712
	ds_write_b16 v122, v59 offset:5984
	ds_write_b16_d16_hi v122, v59 offset:6256
	ds_write_b16 v122, v52 offset:6528
	ds_write_b16_d16_hi v122, v52 offset:6800
	ds_write_b16 v122, v53 offset:7072
	ds_write_b16_d16_hi v122, v53 offset:7344
	ds_write_b16 v122, v54 offset:7616
	ds_write_b16_d16_hi v122, v54 offset:7888
	ds_write_b16 v122, v55 offset:8160
	ds_write_b16_d16_hi v122, v55 offset:8432
	v_mov_b32_e32 v52, s29
	s_waitcnt lgkmcnt(0)
	s_barrier
	ds_read_b32 v97, v52
	ds_read_b32 v52, v112
	ds_read_b32 v53, v111
	v_lshlrev_b32_e32 v54, 16, v48
	v_and_b32_e32 v55, 0xffff0000, v48
	ds_write_b16 v123, v48
	ds_write_b16_d16_hi v124, v48
	s_waitcnt lgkmcnt(3)
	v_sub_f32_e32 v52, v97, v52
	v_exp_f32_e32 v52, v52
	v_mov_b32_e32 v68, 0
	s_andn2_b64 vcc, exec, s[8:9]
	v_mov_b32_e32 v76, 0
	s_waitcnt lgkmcnt(2)
	v_mul_f32_e32 v52, v53, v52
	v_pk_mul_f32 v[54:55], v[52:53], v[54:55] op_sel_hi:[0,1]
	v_cvt_pk_bf16_f32 v48, v54, v55
	ds_write_b16 v125, v48
	ds_write_b16_d16_hi v126, v48
	ds_write_b16 v127, v49
	ds_write_b16_d16_hi v128, v49
	v_lshlrev_b32_e32 v48, 16, v49
	v_and_b32_e32 v49, 0xffff0000, v49
	v_pk_mul_f32 v[48:49], v[52:53], v[48:49] op_sel_hi:[0,1]
	v_cvt_pk_bf16_f32 v48, v48, v49
	ds_write_b16 v129, v48
	ds_write_b16_d16_hi v130, v48
	ds_write_b16 v131, v50
	ds_write_b16_d16_hi v132, v50
	v_lshlrev_b32_e32 v48, 16, v50
	v_and_b32_e32 v49, 0xffff0000, v50
	v_pk_mul_f32 v[48:49], v[52:53], v[48:49] op_sel_hi:[0,1]
	v_cvt_pk_bf16_f32 v48, v48, v49
	ds_write_b16 v133, v48
	ds_write_b16_d16_hi v134, v48
	ds_write_b16 v135, v51
	ds_write_b16_d16_hi v136, v51
	v_lshlrev_b32_e32 v48, 16, v51
	v_and_b32_e32 v49, 0xffff0000, v51
	v_pk_mul_f32 v[48:49], v[52:53], v[48:49] op_sel_hi:[0,1]
	v_cvt_pk_bf16_f32 v48, v48, v49
	ds_write_b16 v137, v48
	ds_write_b16_d16_hi v138, v48
	v_add_u32_e32 v48, v114, v115
	ds_read_b128 v[92:95], v48
	ds_read_b128 v[88:91], v48 offset:64
	ds_read_b128 v[84:87], v48 offset:128
	ds_read_b128 v[80:83], v48 offset:192
	v_cndmask_b32_e64 v48, 0, 1, s[8:9]
	v_cmp_ne_u32_e64 s[74:75], 1, v48
	v_mov_b32_e32 v77, 0
	v_mov_b32_e32 v78, 0
	v_mov_b32_e32 v79, 0
	s_cbranch_vccnz .LBB0_678
	ds_read_b128 v[160:163], v146 offset:34816
	ds_read_b128 v[164:167], v146 offset:34880
	ds_read_b128 v[168:171], v146 offset:34944
	ds_read_b128 v[172:175], v146 offset:35008
	s_waitcnt lgkmcnt(3)
	v_mfma_f32_16x16x32_bf16 v[48:51], v[160:163], v[92:95], 0
	s_waitcnt lgkmcnt(2)
	v_mfma_f32_16x16x32_bf16 v[48:51], v[164:167], v[88:91], v[48:51]
	s_waitcnt lgkmcnt(1)
	v_mfma_f32_16x16x32_bf16 v[48:51], v[168:171], v[84:87], v[48:51]
	s_waitcnt lgkmcnt(0)
	v_mfma_f32_16x16x32_bf16 v[76:79], v[172:175], v[80:83], v[48:51]

; #define LAS __attribute__((address_space(3)))
; __device__ __forceinline__ void ssd_scan_phase(LAS unsigned char* lds, const bf16_t* xbcc, const float* dtb, const float* a_log, const float* dskip, bf16_t* yssd, const int vcu, const int G, const int tid) {
;     ...
;     for (int u = vcu; u < BATCH * SSD_H * 2; u += G) {
;         const int b = u >> 5, h = (u >> 1) & 15, phalf = u & 1, g = h >> 3;
;         const float Ah = -expf(a_log[h]) * 1.4426950408889634f;
;         const float dsk = dskip[h];
;         f32x4 hs[2] = {(f32x4){0.f, 0.f, 0.f, 0.f}, (f32x4){0.f, 0.f, 0.f, 0.f}};
;         for (int i = tid; i < 32 * SP / 2; i += 512) ((LAS unsigned*)hT)[i] = 0u;
;         const int row = tid >> 2, part = tid & 3;
;         u32x4 cvn[4], bvn[4], xrn; float dtn = 0.f, dtn1 = 0.f;
;     ...
;         SS_FETCH(0);
.LBB0_933:
	s_or_b64 exec, exec, s[34:35]
	s_waitcnt vmcnt(10)
	v_mul_f32_e32 v5, 0x3fb8aa3b, v4
	s_lshl_b32 s29, s33, 6
	v_rndne_f32_e32 v6, v5
	s_mov_b32 s33, 0x3fb8aa3b
	v_sub_f32_e32 v7, v5, v6
	v_fma_f32 v5, v4, s33, -v5
	v_fmac_f32_e32 v5, 0x32a5705f, v4
	v_add_f32_e32 v5, v7, v5
	v_exp_f32_e32 v5, v5
	v_cvt_i32_f32_e32 v6, v6
	v_readlane_b32 s31, v255, 8
	s_and_b32 s31, s31, 0xfffff800
	v_readlane_b32 s34, v255, 12
	v_add_u32_e32 v148, s31, v113
	v_add_u32_e32 v149, s31, v140
	v_add_u32_e32 v150, s31, v141
	s_mov_b32 s31, 0xc2ce8ed0
	v_ldexp_f32 v5, v5, v6
	v_cmp_ngt_f32_e32 vcc, s31, v4
	s_mov_b32 s31, 0x42b17218
	v_readlane_b32 s35, v255, 13
	s_add_u32 s30, s34, s30
	v_cndmask_b32_e32 v5, 0, v5, vcc
	v_cmp_nlt_f32_e32 vcc, s31, v4
	s_addc_u32 s31, s35, 0
	s_lshl_b32 s34, s29, 1
	v_readlane_b32 s29, v254, 37
	s_add_u32 s29, s29, s34
	v_readlane_b32 s33, v254, 40
	s_addc_u32 s33, s33, 0
	s_add_u32 s74, s29, s28
	v_cndmask_b32_e32 v4, v242, v5, vcc
	s_addc_u32 s75, s33, 0
	v_mov_b32_e32 v99, v3
	v_mul_f32_e32 v151, 0xbfb8aa3b, v4
	v_lshl_add_u64 v[104:105], s[74:75], 0, v[98:99]
	s_waitcnt vmcnt(9)
	v_mov_b32_e32 v101, v100
	s_mov_b32 s33, 0
	v_mov_b32_e32 v41, v40
	v_mov_b32_e32 v42, v40
	v_mov_b32_e32 v43, v40
	v_mov_b32_e32 v44, v40
	v_mov_b32_e32 v45, v40
	v_mov_b32_e32 v46, v40
	v_mov_b32_e32 v47, v40
	s_movk_i32 s97, 0x3000
	s_waitcnt vmcnt(0)
	s_branch .LBB0_935

; #define LAS __attribute__((address_space(3)))
; #define SS_DPPF(x_, ctrl_, rm_, bc_) __int_as_float(__builtin_amdgcn_update_dpp(0, __float_as_int(x_), (ctrl_), (rm_), 0xF, (bc_)))
; __device__ __forceinline__ void ssd_scan_phase(LAS unsigned char* lds, const bf16_t* xbcc, const float* dtb, const float* a_log, const float* dskip, bf16_t* yssd, const int vcu, const int G, const int tid) {
;     ...
;                 if (wave == 0) {
;                     const float d0 = dtn, d1 = dtn1;
;                     *(LAS f32x2*)(dtv + 2 * lane) = (f32x2){d0, d1};
;                     const float v0 = d0 * Ah, v1 = d1 * Ah;
;                     float s = v0 + v1;
;     ...
;                     s += SS_DPPF(s, 0x111, 0xF, true); asm("" : "+v"(s));
;                     s += SS_DPPF(s, 0x112, 0xF, true); asm("" : "+v"(s));
;                     s += SS_DPPF(s, 0x114, 0xF, true); asm("" : "+v"(s));
;                     s += SS_DPPF(s, 0x118, 0xF, true); asm("" : "+v"(s));
;                     s += SS_DPPF(s, 0x142, 0xA, false); asm("" : "+v"(s));
;                     s += SS_DPPF(s, 0x143, 0xC, false); asm("" : "+v"(s));
;     ...
;                     *(LAS f32x2*)(acum + 2 * lane) = (f32x2){s - v1, s};
;                 }
.LBB0_935:
	s_andn2_b64 vcc, exec, s[2:3]
	s_cbranch_vccnz .LBB0_937
	v_mul_f32_e32 v4, v151, v103
	v_fmac_f32_e32 v4, v151, v102
	v_mov_b32_e32 v5, v3
	ds_write_b64 v108, v[102:103]
	v_add_f32_dpp v4, v4, v4 row_shr:1 row_mask:0xf bank_mask:0xf bound_ctrl:1
	s_nop 1
	v_add_f32_dpp v4, v4, v4 row_shr:2 row_mask:0xf bank_mask:0xf bound_ctrl:1
	s_nop 1
	v_add_f32_dpp v4, v4, v4 row_shr:4 row_mask:0xf bank_mask:0xf bound_ctrl:1
	s_nop 1
	v_add_f32_dpp v4, v4, v4 row_shr:8 row_mask:0xf bank_mask:0xf bound_ctrl:1
	s_nop 1
	v_mov_b32_dpp v5, v4 row_bcast:15 row_mask:0xa bank_mask:0xf
	v_add_f32_e32 v4, v4, v5
	v_mov_b32_e32 v5, v3
	s_nop 1
	v_mov_b32_dpp v5, v4 row_bcast:31 row_mask:0xc bank_mask:0xf
	v_add_f32_e32 v5, v4, v5
	s_nop 0
	v_fma_f32 v4, -v151, v103, v5
	ds_write_b64 v109, v[4:5]

; #define LAS __attribute__((address_space(3)))
; __device__ __forceinline__ unsigned cvt_pk_bf16(float lo, float hi) { const f32x2 v = {lo, hi}; const bf16x2_t b = __builtin_convertvector(v, bf16x2_t); return __builtin_bit_cast(unsigned, b); }
; __device__ __forceinline__ void ssd_scan_phase(LAS unsigned char* lds, const bf16_t* xbcc, const float* dtb, const float* a_log, const float* dskip, bf16_t* yssd, const int vcu, const int G, const int tid) {
;     ...
;                 for (int j = 0; j < 4; ++j) { *(LAS u32x4*)(Cimg + row * SP + 32 * part + 8 * j) = cv[j]; *(LAS u32x4*)(Bimg + row * SP + 32 * part + 8 * j) = bv[j]; }
; #pragma unroll
;                 for (int j = 0; j < 4; ++j) { const unsigned wv[4] = {bv[j].x, bv[j].y, bv[j].z, bv[j].w};
; #pragma unroll
;                     for (int e = 0; e < 4; ++e) { const int n = 32 * part + 8 * j + 2 * e; BTimg[n * SP + row] = (bf16_t)(wv[e] & 0xffffu); BTimg[(n + 1) * SP + row] = (bf16_t)(wv[e] >> 16); } }
;             }
;             __syncthreads();
;             const float atot = acum[127];
;             {
;                 const float wgt = dtv[row] * __builtin_amdgcn_exp2f(atot - acum[row]);
;                 const unsigned wv[4] = {xr.x, xr.y, xr.z, xr.w};
; #pragma unroll
;                 for (int e = 0; e < 4; ++e) { const int p = 8 * part + 2 * e; const float x0 = bf_lo(wv[e]), x1 = bf_hi(wv[e]);
;                     xT[p * SP + row] = (bf16_t)(wv[e] & 0xffffu); xT[(p + 1) * SP + row] = (bf16_t)(wv[e] >> 16);
;                     const unsigned pk = cvt_pk_bf16(x0 * wgt, x1 * wgt); xwT[p * SP + row] = (bf16_t)(pk & 0xffffu); xwT[(p + 1) * SP + row] = (bf16_t)(pk >> 16); }
;             }
;             f32x4 gacc[8];
; #pragma unroll
;             for (int st = 0; st < 8; ++st) gacc[st] = (f32x4){0.f, 0.f, 0.f, 0.f};
;             {
;                 bf16x8 cf[4];
; #pragma unroll
;                 for (int ks = 0; ks < 4; ++ks) cf[ks] = *(const LAS bf16x8*)(Cimg + (16 * lt + fr) * SP + 32 * ks + 8 * fq);
; #pragma unroll
;                 for (int st = 0; st < 8; ++st) if (st <= lt) {
; #pragma unroll
;                     for (int ks = 0; ks < 4; ++ks) { const bf16x8 bfg = *(const LAS bf16x8*)(Bimg + (16 * st + fr) * SP + 32 * ks + 8 * fq);
;                         gacc[st] = __builtin_amdgcn_mfma_f32_16x16x32_bf16(bfg, cf[ks], gacc[st], 0, 0, 0); }
.LBB0_942:
	v_readlane_b32 s29, v253, 56
	ds_write_b128 v110, v[80:83]
	ds_write_b128 v110, v[64:67] offset:34816
	ds_write_b128 v110, v[76:79] offset:16
	ds_write_b128 v110, v[60:63] offset:34832
	ds_write_b128 v110, v[72:75] offset:32
	ds_write_b128 v110, v[56:59] offset:34848
	ds_write_b128 v110, v[68:71] offset:48
	ds_write_b128 v110, v[52:55] offset:34864
	ds_write_b16 v122, v64
	ds_write_b16_d16_hi v122, v64 offset:272
	ds_write_b16 v122, v65 offset:544
	ds_write_b16_d16_hi v122, v65 offset:816
	ds_write_b16 v122, v66 offset:1088
	ds_write_b16_d16_hi v122, v66 offset:1360
	ds_write_b16 v122, v67 offset:1632
	ds_write_b16_d16_hi v122, v67 offset:1904
	ds_write_b16 v122, v60 offset:2176
	ds_write_b16_d16_hi v122, v60 offset:2448
	ds_write_b16 v122, v61 offset:2720
	ds_write_b16_d16_hi v122, v61 offset:2992
	ds_write_b16 v122, v62 offset:3264
	ds_write_b16_d16_hi v122, v62 offset:3536
	ds_write_b16 v122, v63 offset:3808
	ds_write_b16_d16_hi v122, v63 offset:4080
	ds_write_b16 v122, v56 offset:4352
	ds_write_b16_d16_hi v122, v56 offset:4624
	ds_write_b16 v122, v57 offset:4896
	ds_write_b16_d16_hi v122, v57 offset:5168
	ds_write_b16 v122, v58 offset:5440
	ds_write_b16_d16_hi v122, v58 offset:5712
	ds_write_b16 v122, v59 offset:5984
	ds_write_b16_d16_hi v122, v59 offset:6256
	ds_write_b16 v122, v52 offset:6528
	ds_write_b16_d16_hi v122, v52 offset:6800
	ds_write_b16 v122, v53 offset:7072
	ds_write_b16_d16_hi v122, v53 offset:7344
	ds_write_b16 v122, v54 offset:7616
	ds_write_b16_d16_hi v122, v54 offset:7888
	ds_write_b16 v122, v55 offset:8160
	ds_write_b16_d16_hi v122, v55 offset:8432
	v_mov_b32_e32 v52, s29
	s_waitcnt lgkmcnt(0)
	s_barrier
	ds_read_b32 v97, v52
	ds_read_b32 v52, v112
	ds_read_b32 v53, v111
	v_lshlrev_b32_e32 v54, 16, v48
	v_and_b32_e32 v55, 0xffff0000, v48
	ds_write_b16 v123, v48
	ds_write_b16_d16_hi v124, v48
	s_waitcnt lgkmcnt(3)
	v_sub_f32_e32 v52, v97, v52
	v_exp_f32_e32 v52, v52
	v_mov_b32_e32 v64, 0
	s_andn2_b64 vcc, exec, s[8:9]
	v_mov_b32_e32 v76, 0
	s_waitcnt lgkmcnt(2)
	v_mul_f32_e32 v52, v53, v52
	v_pk_mul_f32 v[54:55], v[52:53], v[54:55] op_sel_hi:[0,1]
	v_cvt_pk_bf16_f32 v48, v54, v55
	ds_write_b16 v125, v48
	ds_write_b16_d16_hi v126, v48
	ds_write_b16 v127, v49
	ds_write_b16_d16_hi v128, v49
	v_lshlrev_b32_e32 v48, 16, v49
	v_and_b32_e32 v49, 0xffff0000, v49
	v_pk_mul_f32 v[48:49], v[52:53], v[48:49] op_sel_hi:[0,1]
	v_cvt_pk_bf16_f32 v48, v48, v49
	ds_write_b16 v129, v48
	ds_write_b16_d16_hi v130, v48
	ds_write_b16 v131, v50
	ds_write_b16_d16_hi v132, v50
	v_lshlrev_b32_e32 v48, 16, v50
	v_and_b32_e32 v49, 0xffff0000, v50
	v_pk_mul_f32 v[48:49], v[52:53], v[48:49] op_sel_hi:[0,1]
	v_cvt_pk_bf16_f32 v48, v48, v49
	ds_write_b16 v133, v48
	ds_write_b16_d16_hi v134, v48
	ds_write_b16 v135, v51
	ds_write_b16_d16_hi v136, v51
	v_lshlrev_b32_e32 v48, 16, v51
	v_and_b32_e32 v49, 0xffff0000, v51
	v_pk_mul_f32 v[48:49], v[52:53], v[48:49] op_sel_hi:[0,1]
	v_cvt_pk_bf16_f32 v48, v48, v49
	ds_write_b16 v137, v48
	ds_write_b16_d16_hi v138, v48
	v_add_u32_e32 v48, v114, v115
	ds_read_b128 v[92:95], v48
	ds_read_b128 v[88:91], v48 offset:64
	ds_read_b128 v[84:87], v48 offset:128
	ds_read_b128 v[80:83], v48 offset:192
	v_cndmask_b32_e64 v48, 0, 1, s[8:9]
	v_cmp_ne_u32_e64 s[74:75], 1, v48
	v_mov_b32_e32 v77, 0
	v_mov_b32_e32 v78, 0
	v_mov_b32_e32 v79, 0
	s_cbranch_vccnz .LBB0_944
	ds_read_b128 v[160:163], v145 offset:34816
	ds_read_b128 v[164:167], v145 offset:34880
	ds_read_b128 v[168:171], v145 offset:34944
	ds_read_b128 v[172:175], v145 offset:35008
	s_waitcnt lgkmcnt(3)
	v_mfma_f32_16x16x32_bf16 v[48:51], v[160:163], v[92:95], 0
	s_waitcnt lgkmcnt(2)
	v_mfma_f32_16x16x32_bf16 v[48:51], v[164:167], v[88:91], v[48:51]
	s_waitcnt lgkmcnt(1)
	v_mfma_f32_16x16x32_bf16 v[48:51], v[168:171], v[84:87], v[48:51]
	s_waitcnt lgkmcnt(0)
	v_mfma_f32_16x16x32_bf16 v[76:79], v[172:175], v[80:83], v[48:51]
